# v31 + layer-0 prep copies of the batched weight-quantise passes + layer-0 input-row loop with the next row requested one row ahead
# speedup vs baseline: 1.0069x; 1.0019x over previous
.LBB0_99:
	s_mov_b64 s[14:15], 0
	s_movk_i32 s21, 0x5680
	v_mad_i64_i32 v[132:133], s[12:13], v10, s21, v[6:7]
	v_mov_b32_e32 v18, 0
	v_mov_b32_e32 v19, 0
	s_mov_b32 s22, 0x5680
	s_mov_b32 s23, 0
	s_mov_b32 s17, 8
.Lp1a_max:
	global_load_dword v116, v[132:133], off
	v_lshl_add_u64 v[132:133], v[132:133], 0, s[22:23]
	global_load_dword v117, v[132:133], off
	v_lshl_add_u64 v[132:133], v[132:133], 0, s[22:23]
	global_load_dword v118, v[132:133], off
	v_lshl_add_u64 v[132:133], v[132:133], 0, s[22:23]
	global_load_dword v119, v[132:133], off
	v_lshl_add_u64 v[132:133], v[132:133], 0, s[22:23]
	global_load_dword v120, v[132:133], off
	v_lshl_add_u64 v[132:133], v[132:133], 0, s[22:23]
	global_load_dword v121, v[132:133], off
	v_lshl_add_u64 v[132:133], v[132:133], 0, s[22:23]
	global_load_dword v122, v[132:133], off
	v_lshl_add_u64 v[132:133], v[132:133], 0, s[22:23]
	global_load_dword v123, v[132:133], off
	v_lshl_add_u64 v[132:133], v[132:133], 0, s[22:23]
	global_load_dword v124, v[132:133], off
	v_lshl_add_u64 v[132:133], v[132:133], 0, s[22:23]
	global_load_dword v125, v[132:133], off
	v_lshl_add_u64 v[132:133], v[132:133], 0, s[22:23]
	global_load_dword v126, v[132:133], off
	v_lshl_add_u64 v[132:133], v[132:133], 0, s[22:23]
	global_load_dword v127, v[132:133], off
	v_lshl_add_u64 v[132:133], v[132:133], 0, s[22:23]
	global_load_dword v128, v[132:133], off
	v_lshl_add_u64 v[132:133], v[132:133], 0, s[22:23]
	global_load_dword v129, v[132:133], off
	v_lshl_add_u64 v[132:133], v[132:133], 0, s[22:23]
	global_load_dword v130, v[132:133], off
	v_lshl_add_u64 v[132:133], v[132:133], 0, s[22:23]
	global_load_dword v131, v[132:133], off
	v_lshl_add_u64 v[132:133], v[132:133], 0, s[22:23]
	s_add_i32 s17, s17, -1
	s_waitcnt vmcnt(15)
	v_max_f32_e64 v18, v18, |v116|
	s_waitcnt vmcnt(14)
	v_max_f32_e64 v19, v19, |v117|
	s_waitcnt vmcnt(13)
	v_max_f32_e64 v18, v18, |v118|
	s_waitcnt vmcnt(12)
	v_max_f32_e64 v19, v19, |v119|
	s_waitcnt vmcnt(11)
	v_max_f32_e64 v18, v18, |v120|
	s_waitcnt vmcnt(10)
	v_max_f32_e64 v19, v19, |v121|
	s_waitcnt vmcnt(9)
	v_max_f32_e64 v18, v18, |v122|
	s_waitcnt vmcnt(8)
	v_max_f32_e64 v19, v19, |v123|
	s_waitcnt vmcnt(7)
	v_max_f32_e64 v18, v18, |v124|
	s_waitcnt vmcnt(6)
	v_max_f32_e64 v19, v19, |v125|
	s_waitcnt vmcnt(5)
	v_max_f32_e64 v18, v18, |v126|
	s_waitcnt vmcnt(4)
	v_max_f32_e64 v19, v19, |v127|
	s_waitcnt vmcnt(3)
	v_max_f32_e64 v18, v18, |v128|
	s_waitcnt vmcnt(2)
	v_max_f32_e64 v19, v19, |v129|
	s_waitcnt vmcnt(1)
	v_max_f32_e64 v18, v18, |v130|
	s_waitcnt vmcnt(0)
	v_max_f32_e64 v19, v19, |v131|
	s_cmp_lg_u32 s17, 0
	s_cbranch_scc1 .Lp1a_max
	v_max_f32_e32 v14, v18, v19

.LBB0_110:
	s_nop 1
	v_mov_b32_e32 v4, 0
	v_mov_b32_e32 v5, 0
	v_mov_b32_e32 v6, 0
	v_mov_b32_e32 v7, 0
	s_and_saveexec_b64 s[10:11], s[4:5]
	s_cbranch_execz .LBB0_109
	s_mov_b32 s20, 0xfffaee80
	s_mov_b32 s21, -1
	s_mov_b32 s22, 0x5680
	s_mov_b32 s23, 0
	v_lshl_add_u64 v[132:133], v[16:17], 0, s[20:21]
	global_load_dword v116, v[132:133], off
	v_lshl_add_u64 v[132:133], v[132:133], 0, s[22:23]
	global_load_dword v117, v[132:133], off
	v_lshl_add_u64 v[132:133], v[132:133], 0, s[22:23]
	global_load_dword v118, v[132:133], off
	v_lshl_add_u64 v[132:133], v[132:133], 0, s[22:23]
	global_load_dword v119, v[132:133], off
	v_lshl_add_u64 v[132:133], v[132:133], 0, s[22:23]
	global_load_dword v120, v[132:133], off
	v_lshl_add_u64 v[132:133], v[132:133], 0, s[22:23]
	global_load_dword v121, v[132:133], off
	v_lshl_add_u64 v[132:133], v[132:133], 0, s[22:23]
	global_load_dword v122, v[132:133], off
	v_lshl_add_u64 v[132:133], v[132:133], 0, s[22:23]
	global_load_dword v123, v[132:133], off
	v_lshl_add_u64 v[132:133], v[132:133], 0, s[22:23]
	global_load_dword v124, v[132:133], off
	v_lshl_add_u64 v[132:133], v[132:133], 0, s[22:23]
	global_load_dword v125, v[132:133], off
	v_lshl_add_u64 v[132:133], v[132:133], 0, s[22:23]
	global_load_dword v126, v[132:133], off
	v_lshl_add_u64 v[132:133], v[132:133], 0, s[22:23]
	global_load_dword v127, v[132:133], off
	v_lshl_add_u64 v[132:133], v[132:133], 0, s[22:23]
	global_load_dword v128, v[132:133], off
	v_lshl_add_u64 v[132:133], v[132:133], 0, s[22:23]
	global_load_dword v129, v[132:133], off
	v_lshl_add_u64 v[132:133], v[132:133], 0, s[22:23]
	global_load_dword v130, v[132:133], off
	v_lshl_add_u64 v[132:133], v[132:133], 0, s[22:23]
	global_load_dword v131, v[132:133], off
	s_waitcnt vmcnt(15)
	v_fmaak_f32 v134, v2, v116, 0x43000000
	v_cvt_pk_u8_f32 v4, v134, 0, 0
	s_waitcnt vmcnt(14)
	v_fmaak_f32 v134, v2, v117, 0x43000000
	v_cvt_pk_u8_f32 v4, v134, 1, v4
	s_waitcnt vmcnt(13)
	v_fmaak_f32 v134, v2, v118, 0x43000000
	v_cvt_pk_u8_f32 v4, v134, 2, v4
	s_waitcnt vmcnt(12)
	v_fmaak_f32 v134, v2, v119, 0x43000000
	v_cvt_pk_u8_f32 v4, v134, 3, v4
	v_xor_b32_e32 v4, 0x80808080, v4
	s_waitcnt vmcnt(11)
	v_fmaak_f32 v134, v2, v120, 0x43000000
	v_cvt_pk_u8_f32 v5, v134, 0, 0
	s_waitcnt vmcnt(10)
	v_fmaak_f32 v134, v2, v121, 0x43000000
	v_cvt_pk_u8_f32 v5, v134, 1, v5
	s_waitcnt vmcnt(9)
	v_fmaak_f32 v134, v2, v122, 0x43000000
	v_cvt_pk_u8_f32 v5, v134, 2, v5
	s_waitcnt vmcnt(8)
	v_fmaak_f32 v134, v2, v123, 0x43000000
	v_cvt_pk_u8_f32 v5, v134, 3, v5
	v_xor_b32_e32 v5, 0x80808080, v5
	s_waitcnt vmcnt(7)
	v_fmaak_f32 v134, v2, v124, 0x43000000
	v_cvt_pk_u8_f32 v6, v134, 0, 0
	s_waitcnt vmcnt(6)
	v_fmaak_f32 v134, v2, v125, 0x43000000
	v_cvt_pk_u8_f32 v6, v134, 1, v6
	s_waitcnt vmcnt(5)
	v_fmaak_f32 v134, v2, v126, 0x43000000
	v_cvt_pk_u8_f32 v6, v134, 2, v6
	s_waitcnt vmcnt(4)
	v_fmaak_f32 v134, v2, v127, 0x43000000
	v_cvt_pk_u8_f32 v6, v134, 3, v6
	v_xor_b32_e32 v6, 0x80808080, v6
	s_waitcnt vmcnt(3)
	v_fmaak_f32 v134, v2, v128, 0x43000000
	v_cvt_pk_u8_f32 v7, v134, 0, 0
	s_waitcnt vmcnt(2)
	v_fmaak_f32 v134, v2, v129, 0x43000000
	v_cvt_pk_u8_f32 v7, v134, 1, v7
	s_waitcnt vmcnt(1)
	v_fmaak_f32 v134, v2, v130, 0x43000000
	v_cvt_pk_u8_f32 v7, v134, 2, v7
	s_waitcnt vmcnt(0)
	v_fmaak_f32 v134, v2, v131, 0x43000000
	v_cvt_pk_u8_f32 v7, v134, 3, v7
	v_xor_b32_e32 v7, 0x80808080, v7
	s_branch .LBB0_109

.LBB0_194:
	v_readlane_b32 s0, v254, 11
	s_cmp_lt_i32 s4, 0x10000
	v_readlane_b32 s20, v255, 25
	v_mov_b32_e32 v1, s0
	ds_read_b64 v[4:5], v1
	v_readlane_b32 s21, v253, 42
	s_mov_b32 s16, 0xc000
	s_movk_i32 s17, 0x204
	s_waitcnt lgkmcnt(0)
	v_readfirstlane_b32 s6, v5
	v_readfirstlane_b32 s7, v4
	s_cbranch_scc0 .LBB0_201
	v_and_b32_e32 v1, 64, v242
	v_add_u32_e32 v2, 64, v1
	v_xor_b32_e32 v1, 1, v242
	v_cmp_lt_i32_e32 vcc, v1, v2
	v_xor_b32_e32 v4, 2, v242
	s_add_u32 s10, s18, 0x45200000
	v_cndmask_b32_e32 v1, v242, v1, vcc
	v_cmp_lt_i32_e32 vcc, v4, v2
	s_addc_u32 s11, s19, 0
	s_add_u32 s12, s18, 0x3d600000
	v_cndmask_b32_e32 v4, v242, v4, vcc
	v_lshlrev_b32_e32 v24, 2, v4
	v_xor_b32_e32 v4, 4, v242
	v_cmp_lt_i32_e32 vcc, v4, v2
	s_mov_b64 s[0:1], 0x41200000
	s_addc_u32 s13, s19, 0
	v_cndmask_b32_e32 v4, v242, v4, vcc
	v_lshlrev_b32_e32 v25, 2, v4
	v_xor_b32_e32 v4, 8, v242
	v_cmp_lt_i32_e32 vcc, v4, v2
	s_ashr_i32 s5, s4, 31
	v_mov_b32_e32 v71, v3
	v_cndmask_b32_e32 v4, v242, v4, vcc
	v_lshlrev_b32_e32 v26, 2, v4
	v_xor_b32_e32 v4, 16, v242
	v_cmp_lt_i32_e32 vcc, v4, v2
	v_lshlrev_b32_e32 v1, 2, v1
	v_cmp_eq_u32_e64 s[2:3], 0, v69
	v_cndmask_b32_e32 v4, v242, v4, vcc
	v_lshlrev_b32_e32 v27, 2, v4
	v_xor_b32_e32 v4, 32, v242
	v_cmp_lt_i32_e32 vcc, v4, v2
	s_nop 1
	v_cndmask_b32_e32 v2, v242, v4, vcc
	v_lshlrev_b32_e32 v28, 2, v2
	v_lshlrev_b32_e32 v2, 2, v69
	v_lshl_add_u64 v[4:5], s[18:19], 0, v[2:3]
	v_lshl_add_u64 v[20:21], v[4:5], 0, s[0:1]
	s_lshl_b64 s[0:1], s[4:5], 10
	s_add_u32 s0, s18, s0
	s_addc_u32 s1, s19, s1
	s_add_u32 s0, s0, 0x3e200000
	s_addc_u32 s1, s1, 0
	s_lshl_b64 s[8:9], s[4:5], 12
	s_add_u32 s8, s7, s8
	v_lshlrev_b32_e32 v2, 5, v69
	s_addc_u32 s9, s6, s9
	v_lshl_add_u64 v[4:5], s[8:9], 0, v[2:3]
	s_mov_b64 s[6:7], 0x800
	v_lshl_add_u64 v[22:23], v[4:5], 0, s[6:7]
	global_load_dwordx4 v[116:119], v[22:23], off offset:-2048
	global_load_dwordx4 v[120:123], v[22:23], off offset:-2032
	global_load_dwordx4 v[124:127], v[22:23], off
	global_load_dwordx4 v[128:131], v[22:23], off offset:16
	s_waitcnt vmcnt(0)
	s_branch .LBB0_197

.LBB0_197:
	s_waitcnt vmcnt(4)
	v_mov_b64_e32 v[16:17], v[116:117]
	v_mov_b64_e32 v[18:19], v[118:119]
	v_mov_b64_e32 v[12:13], v[120:121]
	v_mov_b64_e32 v[14:15], v[122:123]
	v_mov_b64_e32 v[8:9], v[124:125]
	v_mov_b64_e32 v[10:11], v[126:127]
	v_mov_b64_e32 v[4:5], v[128:129]
	v_mov_b64_e32 v[6:7], v[130:131]
	s_add_i32 vcc_lo, s4, s94
	s_cmp_gt_i32 vcc_lo, 0xffff
	s_cbranch_scc1 .Lx0_nopf
	v_readlane_b32 vcc_lo, v253, 36
	v_readlane_b32 vcc_hi, v253, 37
	s_nop 1
	v_lshl_add_u64 v[132:133], v[22:23], 0, vcc
	global_load_dwordx4 v[116:119], v[132:133], off offset:-2048
	global_load_dwordx4 v[120:123], v[132:133], off offset:-2032
	global_load_dwordx4 v[124:127], v[132:133], off
	global_load_dwordx4 v[128:131], v[132:133], off offset:16
.Lx0_nopf:
	s_cmpk_gt_i32 s4, 0x3fff
	s_mov_b64 s[6:7], s[4:5]
	s_mov_b64 s[8:9], s[0:1]
	v_max3_f32 v2, |v16|, 0, |v17|
	v_max3_f32 v2, v2, |v18|, |v19|
	v_max3_f32 v2, v2, |v12|, |v13|
	v_max3_f32 v2, v2, |v14|, |v15|
	v_max3_f32 v2, v2, |v8|, |v9|
	v_max3_f32 v2, v2, |v10|, |v11|
	v_max3_f32 v2, v2, |v4|, |v5|
	v_max3_f32 v2, v2, |v6|, |v7|
	ds_bpermute_b32 v29, v1, v2
	s_waitcnt lgkmcnt(0)
	v_max_f32_e32 v29, v29, v29
	v_max_f32_e32 v2, v2, v29
	ds_bpermute_b32 v29, v24, v2
	s_waitcnt lgkmcnt(0)
	v_max_f32_e32 v29, v29, v29
	v_max_f32_e32 v2, v2, v29
	ds_bpermute_b32 v29, v25, v2
	s_waitcnt lgkmcnt(0)
	v_max_f32_e32 v29, v29, v29
	v_max_f32_e32 v2, v2, v29
	ds_bpermute_b32 v29, v26, v2
	s_waitcnt lgkmcnt(0)
	v_max_f32_e32 v29, v29, v29
	v_max_f32_e32 v2, v2, v29
	ds_bpermute_b32 v29, v27, v2
	s_waitcnt lgkmcnt(0)
	v_max_f32_e32 v29, v29, v29
	v_max_f32_e32 v2, v2, v29
	ds_bpermute_b32 v29, v28, v2
	s_cbranch_scc0 .LBB0_199
	s_add_i32 s92, s4, 0xffffc000
	s_lshl_b64 s[6:7], s[92:93], 10
	s_add_u32 s8, s10, s6
	s_mov_b32 s92, s4
	s_addc_u32 s9, s11, s7
	s_mov_b64 s[6:7], s[92:93]

.LBB0_1490:
	s_mov_b64 s[16:17], 0
	s_movk_i32 s23, 0x5680
	v_mad_i64_i32 v[132:133], s[14:15], v10, s23, v[6:7]
	v_mov_b32_e32 v18, 0
	v_mov_b32_e32 v17, 0
	s_mov_b32 s24, 0x5680
	s_mov_b32 s25, 0
	s_mov_b32 s19, 8
.Lp1b_max:
	global_load_dword v116, v[132:133], off
	v_lshl_add_u64 v[132:133], v[132:133], 0, s[24:25]
	global_load_dword v117, v[132:133], off
	v_lshl_add_u64 v[132:133], v[132:133], 0, s[24:25]
	global_load_dword v118, v[132:133], off
	v_lshl_add_u64 v[132:133], v[132:133], 0, s[24:25]
	global_load_dword v119, v[132:133], off
	v_lshl_add_u64 v[132:133], v[132:133], 0, s[24:25]
	global_load_dword v120, v[132:133], off
	v_lshl_add_u64 v[132:133], v[132:133], 0, s[24:25]
	global_load_dword v121, v[132:133], off
	v_lshl_add_u64 v[132:133], v[132:133], 0, s[24:25]
	global_load_dword v122, v[132:133], off
	v_lshl_add_u64 v[132:133], v[132:133], 0, s[24:25]
	global_load_dword v123, v[132:133], off
	v_lshl_add_u64 v[132:133], v[132:133], 0, s[24:25]
	global_load_dword v124, v[132:133], off
	v_lshl_add_u64 v[132:133], v[132:133], 0, s[24:25]
	global_load_dword v125, v[132:133], off
	v_lshl_add_u64 v[132:133], v[132:133], 0, s[24:25]
	global_load_dword v126, v[132:133], off
	v_lshl_add_u64 v[132:133], v[132:133], 0, s[24:25]
	global_load_dword v127, v[132:133], off
	v_lshl_add_u64 v[132:133], v[132:133], 0, s[24:25]
	global_load_dword v128, v[132:133], off
	v_lshl_add_u64 v[132:133], v[132:133], 0, s[24:25]
	global_load_dword v129, v[132:133], off
	v_lshl_add_u64 v[132:133], v[132:133], 0, s[24:25]
	global_load_dword v130, v[132:133], off
	v_lshl_add_u64 v[132:133], v[132:133], 0, s[24:25]
	global_load_dword v131, v[132:133], off
	v_lshl_add_u64 v[132:133], v[132:133], 0, s[24:25]
	s_add_i32 s19, s19, -1
	s_waitcnt vmcnt(15)
	v_max_f32_e64 v18, v18, |v116|
	s_waitcnt vmcnt(14)
	v_max_f32_e64 v17, v17, |v117|
	s_waitcnt vmcnt(13)
	v_max_f32_e64 v18, v18, |v118|
	s_waitcnt vmcnt(12)
	v_max_f32_e64 v17, v17, |v119|
	s_waitcnt vmcnt(11)
	v_max_f32_e64 v18, v18, |v120|
	s_waitcnt vmcnt(10)
	v_max_f32_e64 v17, v17, |v121|
	s_waitcnt vmcnt(9)
	v_max_f32_e64 v18, v18, |v122|
	s_waitcnt vmcnt(8)
	v_max_f32_e64 v17, v17, |v123|
	s_waitcnt vmcnt(7)
	v_max_f32_e64 v18, v18, |v124|
	s_waitcnt vmcnt(6)
	v_max_f32_e64 v17, v17, |v125|
	s_waitcnt vmcnt(5)
	v_max_f32_e64 v18, v18, |v126|
	s_waitcnt vmcnt(4)
	v_max_f32_e64 v17, v17, |v127|
	s_waitcnt vmcnt(3)
	v_max_f32_e64 v18, v18, |v128|
	s_waitcnt vmcnt(2)
	v_max_f32_e64 v17, v17, |v129|
	s_waitcnt vmcnt(1)
	v_max_f32_e64 v18, v18, |v130|
	s_waitcnt vmcnt(0)
	v_max_f32_e64 v17, v17, |v131|
	s_cmp_lg_u32 s19, 0
	s_cbranch_scc1 .Lp1b_max
	v_max_f32_e32 v5, v18, v17
